# COMB row ring: third row waits with vmcnt(8) instead of vmcnt(0), leaving the two reloads just issued in flight
# speedup vs baseline: 1.0087x; 1.0049x over previous
.LBB0_921:
	v_mov_b32_e32 v136, s37
	ds_read_b32 v138, v136 offset:60
	s_and_b64 vcc, exec, s[10:11]
	s_waitcnt vmcnt(8)
	v_mov_b64_e32 v[142:143], v[88:89]
	v_mov_b64_e32 v[140:141], v[90:91]
	v_mov_b64_e32 v[136:137], v[92:93]
	s_waitcnt lgkmcnt(0)
	v_readfirstlane_b32 s10, v138
	v_mov_b64_e32 v[138:139], v[94:95]
	s_cbranch_vccnz .LBB0_923
	v_mov_b32_e32 v136, s37
	ds_read_b32 v136, v136 offset:8
	s_waitcnt lgkmcnt(0)
	v_readfirstlane_b32 s4, v136
	s_ashr_i32 s5, s4, 31
	s_lshl_b64 s[4:5], s[4:5], 11
	v_lshl_add_u64 v[142:143], v[86:87], 0, s[4:5]
	global_load_dwordx2 v[138:139], v[142:143], off nt
	global_load_dwordx2 v[136:137], v[142:143], off offset:512 nt
	global_load_dwordx2 v[140:141], v[142:143], off offset:1024 nt
	s_nop 0
	global_load_dwordx2 v[142:143], v[142:143], off offset:1536 nt
